# QKV epilogue: q/k norm gains requested at the start of the epilogue instead of after the row-sum barrier
# speedup vs baseline: 1.0043x; 1.0043x over previous
;     DI void operator()(const f32x4 (&acc)[2][2][4][2], const Unit& u, int wr, int wc, int fr, int fq) const {
;     ...
; #pragma unroll
;         for (int ai = 0; ai < 2; ++ai)
; #pragma unroll
;             for (int m = 0; m < 4; ++m)
; #pragma unroll
;                 for (int bj = 0; bj < 2; ++bj) { const f32x4 a = acc[ai][bj][m][0], b = acc[ai][bj][m][1];
;                     float s = (a[0] * a[0] + a[1] * a[1]) + (a[2] * a[2] + a[3] * a[3]) + (b[0] * b[0] + b[1] * b[1]) + (b[2] * b[2] + b[3] * b[3]);
;                     s += __shfl_xor(s, 16); s += __shfl_xor(s, 32);
;                     P[((ai * 128 + m * 16 + rl0) * 2 + bj) * 4 + wc] = s; }
;         asm volatile("s_waitcnt lgkmcnt(0)" ::: "memory"); __builtin_amdgcn_s_barrier(); asm volatile("" ::: "memory");
;         constexpr float QSCALE = 0.08838834764831845f * 1.4426950408889634f;
;         int fqo = fq, fro = fr; asm volatile("" : "+v"(fqo), "+v"(fro));
;         const int i0 = 16 * (wc & 1) + 4 * fqo, d0 = 64 * (wc >> 1) + i0;
;         const float* gp = isq ? qg : kg; f32x4 g0 = *(const f32x4*)(gp + d0), g1 = *(const f32x4*)(gp + d0 + 32);
;         if (isq) { g0 = g0 * QSCALE; g1 = g1 * QSCALE; }
.LBB0_1148:
	s_lshl_b32 s21, s0, 8
	v_lshl_add_u32 v2, s87, 8, v207
	s_cmp_lt_i32 s0, 10
	s_mov_b64 s[26:27], -1
	s_mov_b32 s88, s42
	s_cbranch_scc0 .LBB0_1159
	v_readlane_b32 s28, v251, 50
	v_readlane_b32 s29, v251, 51
	v_readlane_b32 s30, v251, 52
	v_readlane_b32 s31, v251, 53
	s_cmp_lt_i32 s0, 8
	s_cselect_b32 s29, s29, s31
	s_cselect_b32 s28, s28, s30
	v_lshl_add_u32 v230, v205, 2, s77
	v_add_u32_e32 v230, s78, v230
	v_lshlrev_b32_e32 v230, 2, v230
	global_load_dwordx4 v[232:235], v230, s[28:29]
	global_load_dwordx4 v[236:239], v230, s[28:29] offset:128
	v_mul_f32_e32 v5, v191, v191
	v_mul_f32_e32 v6, v193, v193
	v_fmac_f32_e32 v5, v190, v190
	v_fmac_f32_e32 v6, v192, v192
	v_and_b32_e32 v4, 64, v223
	v_add_f32_e32 v5, v5, v6
	v_mul_f32_e32 v6, v187, v187
	v_xor_b32_e32 v3, 16, v223
	v_add_u32_e32 v4, 64, v4
	v_fmac_f32_e32 v6, v186, v186
	v_cmp_lt_i32_e32 vcc, v3, v4
	v_add_f32_e32 v5, v5, v6
	v_mul_f32_e32 v6, v189, v189
	v_xor_b32_e32 v7, 32, v223
	v_cndmask_b32_e32 v3, v223, v3, vcc
	v_fmac_f32_e32 v6, v188, v188
	v_cmp_lt_i32_e32 vcc, v7, v4
	v_lshlrev_b32_e32 v3, 2, v3
	v_add_f32_e32 v5, v6, v5
	v_cndmask_b32_e32 v4, v223, v7, vcc
	v_mul_f32_e32 v7, v183, v183
	v_mul_f32_e32 v8, v185, v185
	v_mul_f32_e32 v9, v179, v179
	v_mul_f32_e32 v10, v181, v181
	ds_bpermute_b32 v6, v3, v5
	v_fmac_f32_e32 v7, v182, v182
	v_fmac_f32_e32 v8, v184, v184
	v_fmac_f32_e32 v9, v178, v178
	v_fmac_f32_e32 v10, v180, v180
	v_add_f32_e32 v7, v7, v8
	v_mul_f32_e32 v8, v175, v175
	v_add_f32_e32 v9, v9, v10
	v_mul_f32_e32 v10, v171, v171
	v_fmac_f32_e32 v8, v174, v174
	v_fmac_f32_e32 v10, v170, v170
	v_add_f32_e32 v7, v7, v8
	v_mul_f32_e32 v8, v177, v177
	v_add_f32_e32 v9, v9, v10
	v_mul_f32_e32 v10, v173, v173
	v_fmac_f32_e32 v8, v176, v176
	v_fmac_f32_e32 v10, v172, v172
	v_lshlrev_b32_e32 v4, 2, v4
	s_waitcnt lgkmcnt(0)
	v_add_f32_e32 v5, v5, v6
	v_add_f32_e32 v7, v8, v7
	v_add_f32_e32 v9, v10, v9
	ds_bpermute_b32 v6, v4, v5
	ds_bpermute_b32 v8, v3, v7
	ds_bpermute_b32 v10, v3, v9
	v_mul_f32_e32 v11, v169, v169
	v_fmac_f32_e32 v11, v168, v168
	s_waitcnt lgkmcnt(0)
	v_add_f32_e32 v5, v5, v6
	v_add_f32_e32 v6, v7, v8
	v_add_f32_e32 v8, v9, v10
	v_mul_f32_e32 v10, v167, v167
	v_fmac_f32_e32 v10, v166, v166
	v_add_f32_e32 v10, v10, v11
	v_mul_f32_e32 v11, v159, v159
	v_fmac_f32_e32 v11, v158, v158
	v_add_f32_e32 v10, v10, v11
	v_mul_f32_e32 v11, v161, v161
	v_fmac_f32_e32 v11, v160, v160
	ds_bpermute_b32 v7, v4, v6
	v_add_f32_e32 v10, v11, v10
	ds_bpermute_b32 v9, v4, v8
	ds_bpermute_b32 v11, v3, v10
	v_add_u32_e32 v12, s79, v217
	s_waitcnt lgkmcnt(0)
	v_add_f32_e32 v6, v6, v7
	ds_write2_b32 v12, v5, v6 offset1:4
	v_add_f32_e32 v5, v8, v9
	v_add_f32_e32 v6, v10, v11
	v_mul_f32_e32 v8, v163, v163
	v_mul_f32_e32 v9, v165, v165
	v_mul_f32_e32 v10, v151, v151
	v_mul_f32_e32 v11, v153, v153
	v_fmac_f32_e32 v8, v162, v162
	v_fmac_f32_e32 v9, v164, v164
	v_fmac_f32_e32 v10, v150, v150
	v_fmac_f32_e32 v11, v152, v152
	v_add_f32_e32 v8, v8, v9
	v_mul_f32_e32 v9, v155, v155
	v_add_f32_e32 v10, v10, v11
	v_mul_f32_e32 v11, v143, v143
	v_fmac_f32_e32 v9, v154, v154
	v_fmac_f32_e32 v11, v142, v142
	v_add_f32_e32 v8, v8, v9
	v_mul_f32_e32 v9, v157, v157
	v_add_f32_e32 v10, v10, v11
	v_mul_f32_e32 v11, v145, v145
	v_fmac_f32_e32 v9, v156, v156
	v_fmac_f32_e32 v11, v144, v144
	ds_bpermute_b32 v7, v4, v6
	v_add_f32_e32 v8, v9, v8
	v_add_f32_e32 v10, v11, v10
	ds_bpermute_b32 v9, v3, v8
	ds_bpermute_b32 v11, v3, v10
	s_waitcnt lgkmcnt(0)
	v_add_f32_e32 v6, v6, v7
	ds_write2_b32 v12, v5, v6 offset0:128 offset1:132
	v_mul_f32_e32 v13, v119, v119
	v_add_f32_e32 v5, v8, v9
	v_add_f32_e32 v7, v10, v11
	v_mul_f32_e32 v9, v147, v147
	v_mul_f32_e32 v10, v149, v149
	v_fmac_f32_e32 v9, v146, v146
	v_fmac_f32_e32 v10, v148, v148
	v_add_f32_e32 v9, v9, v10
	v_mul_f32_e32 v10, v139, v139
	v_fmac_f32_e32 v10, v138, v138
	v_add_f32_e32 v9, v9, v10
	v_mul_f32_e32 v10, v141, v141
	v_fmac_f32_e32 v10, v140, v140
	ds_bpermute_b32 v6, v4, v5
	ds_bpermute_b32 v8, v4, v7
	v_add_f32_e32 v9, v10, v9
	ds_bpermute_b32 v10, v3, v9
	v_mul_f32_e32 v11, v129, v129
	s_waitcnt lgkmcnt(0)
	v_add_f32_e32 v5, v5, v6
	v_add_f32_e32 v6, v7, v8
	v_add_u32_e32 v7, 0x400, v12
	ds_write2_b32 v7, v5, v6 offset1:4
	v_add_f32_e32 v5, v9, v10
	v_mul_f32_e32 v8, v135, v135
	v_mul_f32_e32 v9, v137, v137
	v_fmac_f32_e32 v8, v134, v134
	v_fmac_f32_e32 v9, v136, v136
	v_mul_f32_e32 v10, v127, v127
	v_add_f32_e32 v8, v8, v9
	v_mul_f32_e32 v9, v131, v131
	v_fmac_f32_e32 v10, v126, v126
	v_fmac_f32_e32 v11, v128, v128
	v_fmac_f32_e32 v9, v130, v130
	v_add_f32_e32 v10, v10, v11
	v_mul_f32_e32 v11, v123, v123
	v_add_f32_e32 v8, v8, v9
	v_mul_f32_e32 v9, v133, v133
	v_fmac_f32_e32 v11, v122, v122
	v_fmac_f32_e32 v9, v132, v132
	v_add_f32_e32 v10, v10, v11
	v_mul_f32_e32 v11, v125, v125
	v_add_f32_e32 v8, v9, v8
	v_fmac_f32_e32 v11, v124, v124
	ds_bpermute_b32 v9, v3, v8
	v_add_f32_e32 v10, v11, v10
	ds_bpermute_b32 v11, v3, v10
	ds_bpermute_b32 v6, v4, v5
	v_mul_f32_e32 v14, v121, v121
	s_waitcnt lgkmcnt(0)
	v_add_f32_e32 v8, v8, v9
	ds_bpermute_b32 v9, v4, v8
	v_add_f32_e32 v10, v10, v11
	ds_bpermute_b32 v11, v4, v10
	v_add_f32_e32 v5, v5, v6
	v_fmac_f32_e32 v13, v118, v118
	s_waitcnt lgkmcnt(0)
;     DI void operator()(const f32x4 (&acc)[2][2][4][2], const Unit& u, int wr, int wc, int fr, int fq) const {
;     ...
;                 for (int bj = 0; bj < 2; ++bj) { const f32x4 a = acc[ai][bj][m][0], b = acc[ai][bj][m][1];
;                     float s = (a[0] * a[0] + a[1] * a[1]) + (a[2] * a[2] + a[3] * a[3]) + (b[0] * b[0] + b[1] * b[1]) + (b[2] * b[2] + b[3] * b[3]);
;                     s += __shfl_xor(s, 16); s += __shfl_xor(s, 32);
;                     P[((ai * 128 + m * 16 + rl0) * 2 + bj) * 4 + wc] = s; }
;         asm volatile("s_waitcnt lgkmcnt(0)" ::: "memory"); __builtin_amdgcn_s_barrier(); asm volatile("" ::: "memory");
;         constexpr float QSCALE = 0.08838834764831845f * 1.4426950408889634f;
;         int fqo = fq, fro = fr; asm volatile("" : "+v"(fqo), "+v"(fro));
;         const int i0 = 16 * (wc & 1) + 4 * fqo, d0 = 64 * (wc >> 1) + i0;
;         const float* gp = isq ? qg : kg; f32x4 g0 = *(const f32x4*)(gp + d0), g1 = *(const f32x4*)(gp + d0 + 32);
;         if (isq) { g0 = g0 * QSCALE; g1 = g1 * QSCALE; }
	v_add_f32_e32 v6, v8, v9
	v_fmac_f32_e32 v14, v120, v120
	ds_write2_b32 v7, v5, v6 offset0:128 offset1:132
	v_add_f32_e32 v5, v10, v11
	v_mul_f32_e32 v8, v115, v115
	v_mul_f32_e32 v9, v117, v117
	v_mul_f32_e32 v10, v87, v87
	v_mul_f32_e32 v11, v89, v89
	v_add_f32_e32 v13, v13, v14
	v_mul_f32_e32 v14, v111, v111
	v_fmac_f32_e32 v8, v114, v114
	v_fmac_f32_e32 v9, v116, v116
	v_fmac_f32_e32 v10, v86, v86
	v_fmac_f32_e32 v11, v88, v88
	v_fmac_f32_e32 v14, v110, v110
	v_add_f32_e32 v8, v8, v9
	v_mul_f32_e32 v9, v107, v107
	v_add_f32_e32 v10, v10, v11
	v_mul_f32_e32 v11, v75, v75
	v_add_f32_e32 v13, v13, v14
	v_mul_f32_e32 v14, v113, v113
	v_fmac_f32_e32 v9, v106, v106
	v_fmac_f32_e32 v11, v74, v74
	v_fmac_f32_e32 v14, v112, v112
	v_add_f32_e32 v8, v8, v9
	v_mul_f32_e32 v9, v109, v109
	v_add_f32_e32 v10, v10, v11
	v_mul_f32_e32 v11, v77, v77
	v_add_f32_e32 v13, v14, v13
	v_fmac_f32_e32 v9, v108, v108
	v_fmac_f32_e32 v11, v76, v76
	ds_bpermute_b32 v14, v3, v13
	v_add_f32_e32 v8, v9, v8
	v_add_f32_e32 v10, v11, v10
	ds_bpermute_b32 v9, v3, v8
	ds_bpermute_b32 v11, v3, v10
	s_waitcnt lgkmcnt(0)
	v_add_f32_e32 v13, v13, v14
	ds_bpermute_b32 v14, v4, v13
	v_add_u32_e32 v7, 0x1000, v12
	v_add_f32_e32 v8, v8, v9
	v_add_f32_e32 v10, v10, v11
	ds_bpermute_b32 v9, v4, v8
	ds_bpermute_b32 v11, v4, v10
	s_waitcnt lgkmcnt(0)
	v_add_f32_e32 v6, v13, v14
	ds_write2_b32 v7, v5, v6 offset1:4
	v_mul_f32_e32 v13, v83, v83
	v_add_f32_e32 v5, v8, v9
	v_add_f32_e32 v6, v10, v11
	v_mul_f32_e32 v14, v85, v85
	ds_write2_b32 v7, v5, v6 offset0:128 offset1:132
	v_mul_f32_e32 v6, v99, v99
	v_mul_f32_e32 v7, v101, v101
	v_fmac_f32_e32 v13, v82, v82
	v_fmac_f32_e32 v14, v84, v84
	v_fmac_f32_e32 v6, v98, v98
	v_fmac_f32_e32 v7, v100, v100
	v_mul_f32_e32 v8, v71, v71
	v_mul_f32_e32 v9, v73, v73
	v_mul_f32_e32 v10, v91, v91
	v_mul_f32_e32 v11, v93, v93
	v_add_f32_e32 v13, v13, v14
	v_mul_f32_e32 v14, v79, v79
	v_add_f32_e32 v6, v6, v7
	v_mul_f32_e32 v7, v103, v103
	v_fmac_f32_e32 v8, v70, v70
	v_fmac_f32_e32 v9, v72, v72
	v_fmac_f32_e32 v10, v90, v90
	v_fmac_f32_e32 v11, v92, v92
	v_fmac_f32_e32 v14, v78, v78
	v_fmac_f32_e32 v7, v102, v102
	v_add_f32_e32 v8, v8, v9
	v_mul_f32_e32 v9, v67, v67
	v_add_f32_e32 v10, v10, v11
	v_mul_f32_e32 v11, v95, v95
	v_add_f32_e32 v13, v13, v14
	v_mul_f32_e32 v14, v81, v81
	v_add_f32_e32 v6, v6, v7
	v_mul_f32_e32 v7, v105, v105
	v_fmac_f32_e32 v9, v66, v66
	v_fmac_f32_e32 v11, v94, v94
	v_fmac_f32_e32 v14, v80, v80
	v_fmac_f32_e32 v7, v104, v104
	v_add_f32_e32 v8, v8, v9
	v_mul_f32_e32 v9, v69, v69
	v_add_f32_e32 v10, v10, v11
	v_mul_f32_e32 v11, v97, v97
	v_add_f32_e32 v13, v14, v13
	v_add_f32_e32 v6, v7, v6
	v_fmac_f32_e32 v9, v68, v68
	v_fmac_f32_e32 v11, v96, v96
	ds_bpermute_b32 v14, v3, v13
	ds_bpermute_b32 v7, v3, v6
	v_add_f32_e32 v8, v9, v8
	v_add_f32_e32 v10, v11, v10
	ds_bpermute_b32 v9, v3, v8
	ds_bpermute_b32 v3, v3, v10
	s_waitcnt lgkmcnt(0)
	v_add_f32_e32 v13, v13, v14
	v_add_f32_e32 v6, v6, v7
	ds_bpermute_b32 v14, v4, v13
	ds_bpermute_b32 v7, v4, v6
	v_add_f32_e32 v8, v8, v9
	v_add_f32_e32 v3, v10, v3
	ds_bpermute_b32 v9, v4, v8
	ds_bpermute_b32 v4, v4, v3
	s_waitcnt lgkmcnt(0)
	v_add_f32_e32 v5, v13, v14
	v_add_f32_e32 v6, v6, v7
	v_add_u32_e32 v7, 0x1400, v12
	s_add_i32 s26, s21, 0xfffff800
	ds_write2_b32 v7, v5, v6 offset1:4
	v_add_f32_e32 v5, v8, v9
	v_add_f32_e32 v3, v3, v4
	s_cmp_lt_i32 s0, 8
	ds_write2_b32 v7, v5, v3 offset0:128 offset1:132
	v_mov_b32_e32 v3, v205
	v_mov_b32_e32 v16, v197
	s_cselect_b64 s[0:1], -1, 0
	s_waitcnt lgkmcnt(0)
	s_barrier
	v_readlane_b32 s40, v251, 42
	s_and_b64 s[28:29], s[0:1], exec
	v_lshl_add_u32 v3, v3, 2, s77
	v_readlane_b32 s48, v251, 50
	v_readlane_b32 s49, v251, 51
	v_readlane_b32 s50, v251, 52
	v_readlane_b32 s51, v251, 53
	v_add_u32_e32 v4, s78, v3
	s_cselect_b32 s27, s49, s51
	s_cselect_b32 s28, s48, s50
	v_mov_b32_e32 v6, s28
	v_mov_b32_e32 v7, s27
	v_ashrrev_i32_e32 v5, 31, v4
	v_lshl_add_u64 v[4:5], v[4:5], 2, v[6:7]
	s_nop 0
	s_nop 0
	v_readlane_b32 s28, v251, 38
	v_readlane_b32 s29, v251, 39
	s_cselect_b32 s30, s65, s29
	s_cselect_b32 s31, s64, s28
	s_cselect_b32 s26, s21, s26
	s_mov_b64 s[28:29], -1
	s_cmp_gt_i32 s87, 63
	v_readlane_b32 s41, v251, 43
	v_readlane_b32 s42, v251, 44
	v_readlane_b32 s43, v251, 45
	v_readlane_b32 s44, v251, 46
	v_readlane_b32 s45, v251, 47
	v_readlane_b32 s46, v251, 48
	v_readlane_b32 s47, v251, 49
	v_readlane_b32 s52, v251, 54
	v_readlane_b32 s53, v251, 55
	v_readlane_b32 s54, v251, 56
	v_readlane_b32 s55, v251, 57
	s_waitcnt vmcnt(0)
	v_pk_mul_f32 v[12:13], v[234:235], s[16:17] op_sel_hi:[1,0]
	v_pk_mul_f32 v[14:15], v[232:233], s[16:17] op_sel_hi:[1,0]
	v_pk_mul_f32 v[18:19], v[238:239], s[16:17] op_sel_hi:[1,0]
	v_pk_mul_f32 v[20:21], v[236:237], s[16:17] op_sel_hi:[1,0]
	v_cndmask_b32_e64 v7, v239, v19, s[0:1]
	v_cndmask_b32_e64 v5, v237, v21, s[0:1]
	v_cndmask_b32_e64 v4, v236, v20, s[0:1]
	v_cndmask_b32_e64 v6, v238, v18, s[0:1]
	v_cndmask_b32_e64 v9, v233, v15, s[0:1]
	v_cndmask_b32_e64 v8, v232, v14, s[0:1]
	v_cndmask_b32_e64 v11, v235, v13, s[0:1]
	v_cndmask_b32_e64 v10, v234, v12, s[0:1]
	v_lshlrev_b32_e32 v12, 1, v210
	s_cbranch_scc1 .LBB0_1155
;     DI void operator()(const f32x4 (&acc)[2][2][4][2], const Unit& u, int wr, int wc, int fr, int fq) const {
;     ...
;         if (u.pm >= 64) {
;             const f32x4 one = (f32x4){1.f, 1.f, 1.f, 1.f}, zero = (f32x4){0.f, 0.f, 0.f, 0.f};
; #pragma unroll
;             for (int ai = 0; ai < 2; ++ai)
; #pragma unroll
;                 for (int m = 0; m < 4; ++m) QKV_OUT(ai, m, one, zero);
;             return;
;         }
;         f32x4 ifr;
; #pragma unroll
;         for (int j = 0; j < 4; ++j) ifr[j] = exp2f(-(float)(i0 + j) * (13.287712379549449f / 32.0f)) * 0.15915494309189535f;
;         if ((wc >> 1) == 0) {
; #pragma unroll
;             for (int ai = 0; ai < 2; ++ai) { const float pos = (float)((4 * u.pm + wr + 2 * ai) & 31); f32x4 cs, sn;
; #pragma unroll
;                 for (int j = 0; j < 4; ++j) { const float rev = pos * ifr[j]; cs[j] = __builtin_amdgcn_cosf(rev); sn[j] = __builtin_amdgcn_sinf(rev); }
; #pragma unroll
;                 for (int m = 0; m < 4; ++m) QKV_OUT(ai, m, cs, sn); }
;         } else {
; #pragma unroll
;             for (int m = 0; m < 4; ++m) { const float pos = (float)(16 * m + fro); f32x4 cs, sn;
; #pragma unroll
;                 for (int j = 0; j < 4; ++j) { const float rev = pos * ifr[j]; cs[j] = __builtin_amdgcn_cosf(rev); sn[j] = __builtin_amdgcn_sinf(rev); }
; #pragma unroll
;                 for (int ai = 0; ai < 2; ++ai) QKV_OUT(ai, m, cs, sn); }
	v_cvt_f32_i32_e32 v13, v3
	v_or_b32_e32 v14, 1, v3
	v_cvt_f32_i32_e32 v14, v14
	s_and_b64 s[28:29], s[0:1], exec
	v_mul_f32_e32 v15, 0xbed49a78, v13
	v_cmp_gt_f32_e32 vcc, s84, v15
	s_cselect_b32 s34, 11, 9
	s_ashr_i32 s27, s26, 31
	v_cndmask_b32_e32 v17, 0, v225, vcc
	v_fmac_f32_e32 v17, 0xbed49a78, v13
	v_exp_f32_e32 v13, v17
	v_mul_f32_e32 v17, 0xbed49a78, v14
	v_cndmask_b32_e32 v15, 0, v224, vcc
	v_cmp_gt_f32_e32 vcc, s84, v17
	v_ldexp_f32 v13, v13, v15
	v_mul_f32_e32 v24, 0.15915494, v13
	v_cndmask_b32_e32 v17, 0, v225, vcc
	v_fmac_f32_e32 v17, 0xbed49a78, v14
	v_exp_f32_e32 v13, v17
	v_or_b32_e32 v14, 2, v3
	v_cvt_f32_i32_e32 v14, v14
	v_or_b32_e32 v3, 3, v3
	v_cndmask_b32_e32 v15, 0, v224, vcc
	v_cvt_f32_i32_e32 v3, v3
	v_ldexp_f32 v13, v13, v15
	v_mul_f32_e32 v26, 0.15915494, v13
	v_mul_f32_e32 v13, 0xbed49a78, v14
	v_cmp_gt_f32_e32 vcc, s84, v13
	v_mul_f32_e32 v15, 0xbed49a78, v3
	s_lshl_b64 s[28:29], s[26:27], 1
	v_cndmask_b32_e32 v13, 0, v225, vcc
	v_fmac_f32_e32 v13, 0xbed49a78, v14
	v_cndmask_b32_e32 v14, 0, v224, vcc
	v_cmp_gt_f32_e32 vcc, s84, v15
	v_exp_f32_e32 v13, v13
	s_add_u32 s27, s31, s28
	v_cndmask_b32_e32 v15, 0, v225, vcc
	v_fmac_f32_e32 v15, 0xbed49a78, v3
	v_exp_f32_e32 v3, v15
	v_ldexp_f32 v13, v13, v14
	s_addc_u32 s29, s30, s29
	s_lshl_b32 s28, s74, 1
	v_mul_f32_e32 v27, 0.15915494, v13
	v_cndmask_b32_e32 v13, 0, v224, vcc
	s_add_u32 s28, s27, s28
	v_ldexp_f32 v3, v3, v13
	s_addc_u32 s29, s29, 0
	v_mov_b32_e32 v13, v203
	v_mul_f32_e32 v25, 0.15915494, v3
	v_lshl_add_u64 v[14:15], s[28:29], 0, v[12:13]
	s_mov_b64 s[28:29], -1
	s_and_b64 vcc, exec, s[14:15]
	s_cbranch_vccz .LBB0_1152
	v_cvt_f32_i32_e32 v3, v16
	v_mul_f32_e32 v13, v24, v3
	v_cos_f32_e32 v22, v13
	v_sin_f32_e32 v32, v13
	v_add_u32_e32 v13, 0, v217
	v_add_u32_e32 v13, 0x20000, v13
	ds_read_b128 v[18:21], v13
	v_mul_f32_e32 v17, v26, v3
	v_cos_f32_e32 v23, v17
	v_sin_f32_e32 v33, v17
	v_mul_f32_e32 v17, v27, v3
	s_waitcnt lgkmcnt(0)
	v_mov_b32_e32 v28, v19
	v_mov_b32_e32 v29, v20
	v_mov_b32_e32 v19, v21
	v_pk_add_f32 v[18:19], v[28:29], v[18:19]
	v_cos_f32_e32 v34, v17
	v_sin_f32_e32 v36, v17
	v_add_f32_e32 v17, v18, v19
	v_fmamk_f32 v17, v17, 0x37000000, v222
	v_rsq_f32_e32 v17, v17
	v_mul_f32_e32 v3, v25, v3
	v_sin_f32_e32 v37, v3
	v_cos_f32_e32 v35, v3
	v_mul_f32_e32 v18, 0x3d000000, v17
	v_pk_mul_f32 v[20:21], v[10:11], v[18:19] op_sel_hi:[1,0]
	v_pk_mul_f32 v[28:29], v[8:9], v[18:19] op_sel_hi:[1,0]
	v_pk_mul_f32 v[30:31], v[4:5], v[18:19] op_sel_hi:[1,0]
	v_pk_mul_f32 v[18:19], v[6:7], v[18:19] op_sel_hi:[1,0]
	v_pk_mul_f32 v[30:31], v[186:187], v[30:31]
	v_pk_mul_f32 v[18:19], v[188:189], v[18:19]
	v_pk_mul_f32 v[28:29], v[190:191], v[28:29]
	v_pk_mul_f32 v[20:21], v[192:193], v[20:21]
	v_pk_mul_f32 v[38:39], v[32:33], v[30:31]
	v_pk_mul_f32 v[40:41], v[36:37], v[18:19]
	v_pk_fma_f32 v[38:39], v[22:23], v[28:29], v[38:39] neg_lo:[0,0,1] neg_hi:[0,0,1]
	v_pk_fma_f32 v[40:41], v[34:35], v[20:21], v[40:41] neg_lo:[0,0,1] neg_hi:[0,0,1]
	v_pk_mul_f32 v[28:29], v[32:33], v[28:29]
	v_pk_mul_f32 v[20:21], v[36:37], v[20:21]
	v_ashrrev_i32_e32 v3, 31, v2
	v_pk_fma_f32 v[42:43], v[34:35], v[18:19], v[20:21]
	v_pk_fma_f32 v[20:21], v[22:23], v[30:31], v[28:29]
	v_cvt_pk_bf16_f32 v18, v38, v39
	v_cvt_pk_bf16_f32 v19, v40, v41
	s_nop 0
	v_cvt_pk_bf16_f32 v20, v20, v21
	v_cvt_pk_bf16_f32 v21, v42, v43
	ds_read_b128 v[28:31], v13 offset:16
	s_waitcnt lgkmcnt(0)
	v_mov_b32_e32 v38, v29
	v_mov_b32_e32 v39, v30
	v_mov_b32_e32 v29, v31
	v_pk_add_f32 v[28:29], v[38:39], v[28:29]
	s_nop 0
	v_add_f32_e32 v17, v28, v29
	v_fmamk_f32 v17, v17, 0x37000000, v222
	v_rsq_f32_e32 v17, v17
	v_lshlrev_b64 v[28:29], s34, v[2:3]
	v_lshl_add_u64 v[28:29], v[28:29], 1, v[14:15]
	global_store_dwordx4 v[28:29], v[18:21], off
	s_nop 1
	v_mul_f32_e32 v18, 0x3d000000, v17
	v_pk_mul_f32 v[20:21], v[10:11], v[18:19] op_sel_hi:[1,0]
	v_pk_mul_f32 v[30:31], v[8:9], v[18:19] op_sel_hi:[1,0]
	v_pk_mul_f32 v[38:39], v[4:5], v[18:19] op_sel_hi:[1,0]
	v_pk_mul_f32 v[18:19], v[6:7], v[18:19] op_sel_hi:[1,0]
	v_pk_mul_f32 v[38:39], v[174:175], v[38:39]
	v_pk_mul_f32 v[18:19], v[176:177], v[18:19]
	v_pk_mul_f32 v[30:31], v[182:183], v[30:31]
	v_pk_mul_f32 v[20:21], v[184:185], v[20:21]
	v_pk_mul_f32 v[40:41], v[32:33], v[38:39]
	v_pk_mul_f32 v[42:43], v[36:37], v[18:19]
	v_pk_fma_f32 v[40:41], v[22:23], v[30:31], v[40:41] neg_lo:[0,0,1] neg_hi:[0,0,1]
	v_pk_fma_f32 v[42:43], v[34:35], v[20:21], v[42:43] neg_lo:[0,0,1] neg_hi:[0,0,1]
	v_pk_mul_f32 v[30:31], v[32:33], v[30:31]
	v_pk_mul_f32 v[20:21], v[36:37], v[20:21]
	s_nop 0
	v_pk_fma_f32 v[44:45], v[34:35], v[18:19], v[20:21]
	v_pk_fma_f32 v[20:21], v[22:23], v[38:39], v[30:31]
	v_cvt_pk_bf16_f32 v18, v40, v41
	v_cvt_pk_bf16_f32 v19, v42, v43
	s_nop 0
	v_cvt_pk_bf16_f32 v20, v20, v21
	v_cvt_pk_bf16_f32 v21, v44, v45
	global_store_dwordx4 v[28:29], v[18:21], off offset:256
	ds_read_b128 v[18:21], v13 offset:4096
	s_waitcnt lgkmcnt(0)
	v_mov_b32_e32 v28, v19
	v_mov_b32_e32 v29, v20
	v_mov_b32_e32 v19, v21
	v_pk_add_f32 v[18:19], v[28:29], v[18:19]
	s_nop 0
	v_add_f32_e32 v3, v18, v19
	v_fmamk_f32 v3, v3, 0x37000000, v222
	v_rsq_f32_e32 v3, v3
	s_nop 0
	v_mul_f32_e32 v18, 0x3d000000, v3
	v_pk_mul_f32 v[20:21], v[10:11], v[18:19] op_sel_hi:[1,0]
	v_pk_mul_f32 v[28:29], v[8:9], v[18:19] op_sel_hi:[1,0]
	v_pk_mul_f32 v[30:31], v[4:5], v[18:19] op_sel_hi:[1,0]
	v_pk_mul_f32 v[18:19], v[6:7], v[18:19] op_sel_hi:[1,0]
	v_pk_mul_f32 v[30:31], v[122:123], v[30:31]
	v_pk_mul_f32 v[18:19], v[124:125], v[18:19]
	v_pk_mul_f32 v[28:29], v[126:127], v[28:29]
	v_pk_mul_f32 v[20:21], v[128:129], v[20:21]
	v_pk_mul_f32 v[38:39], v[32:33], v[30:31]
	v_pk_mul_f32 v[40:41], v[36:37], v[18:19]
	v_pk_fma_f32 v[38:39], v[22:23], v[28:29], v[38:39] neg_lo:[0,0,1] neg_hi:[0,0,1]
	v_pk_fma_f32 v[40:41], v[34:35], v[20:21], v[40:41] neg_lo:[0,0,1] neg_hi:[0,0,1]
	v_pk_mul_f32 v[28:29], v[32:33], v[28:29]
	v_pk_mul_f32 v[20:21], v[36:37], v[20:21]
	s_nop 0
	v_pk_fma_f32 v[42:43], v[34:35], v[18:19], v[20:21]
	v_pk_fma_f32 v[20:21], v[22:23], v[30:31], v[28:29]
	v_cvt_pk_bf16_f32 v18, v38, v39
	v_cvt_pk_bf16_f32 v19, v40, v41
	v_add_u32_e32 v38, 0x80, v2
	v_cvt_pk_bf16_f32 v20, v20, v21
	v_cvt_pk_bf16_f32 v21, v42, v43
	ds_read_b128 v[28:31], v13 offset:4112
	v_ashrrev_i32_e32 v39, 31, v38
	s_waitcnt lgkmcnt(0)
;     DI void operator()(const f32x4 (&acc)[2][2][4][2], const Unit& u, int wr, int wc, int fr, int fq) const {
;     ...
;             for (int m = 0; m < 4; ++m) { const float pos = (float)(16 * m + fro); f32x4 cs, sn;
; #pragma unroll
;                 for (int j = 0; j < 4; ++j) { const float rev = pos * ifr[j]; cs[j] = __builtin_amdgcn_cosf(rev); sn[j] = __builtin_amdgcn_sinf(rev); }
; #pragma unroll
;                 for (int ai = 0; ai < 2; ++ai) QKV_OUT(ai, m, cs, sn); }
	v_mov_b32_e32 v40, v29
	v_mov_b32_e32 v41, v30
	v_mov_b32_e32 v29, v31
	v_pk_add_f32 v[28:29], v[40:41], v[28:29]
	s_nop 0
	v_add_f32_e32 v3, v28, v29
	v_fmamk_f32 v3, v3, 0x37000000, v222
	v_rsq_f32_e32 v3, v3
	v_lshlrev_b64 v[28:29], s34, v[38:39]
	v_lshl_add_u64 v[28:29], v[28:29], 1, v[14:15]
	global_store_dwordx4 v[28:29], v[18:21], off
	s_nop 1
	v_mul_f32_e32 v18, 0x3d000000, v3
	v_pk_mul_f32 v[20:21], v[10:11], v[18:19] op_sel_hi:[1,0]
	v_pk_mul_f32 v[30:31], v[8:9], v[18:19] op_sel_hi:[1,0]
	v_pk_mul_f32 v[38:39], v[4:5], v[18:19] op_sel_hi:[1,0]
	v_pk_mul_f32 v[18:19], v[6:7], v[18:19] op_sel_hi:[1,0]
	v_pk_mul_f32 v[38:39], v[110:111], v[38:39]
	v_pk_mul_f32 v[18:19], v[112:113], v[18:19]
	v_pk_mul_f32 v[30:31], v[118:119], v[30:31]
	v_pk_mul_f32 v[20:21], v[120:121], v[20:21]
	v_pk_mul_f32 v[40:41], v[32:33], v[38:39]
	v_pk_mul_f32 v[42:43], v[36:37], v[18:19]
	v_pk_fma_f32 v[40:41], v[22:23], v[30:31], v[40:41] neg_lo:[0,0,1] neg_hi:[0,0,1]
	v_pk_fma_f32 v[42:43], v[34:35], v[20:21], v[42:43] neg_lo:[0,0,1] neg_hi:[0,0,1]
	v_pk_mul_f32 v[30:31], v[32:33], v[30:31]
	v_pk_mul_f32 v[20:21], v[36:37], v[20:21]
	s_nop 0
	v_pk_fma_f32 v[32:33], v[34:35], v[18:19], v[20:21]
	v_pk_fma_f32 v[20:21], v[22:23], v[38:39], v[30:31]
	v_cvt_pk_bf16_f32 v18, v40, v41
	v_cvt_pk_bf16_f32 v19, v42, v43
	s_nop 0
	v_cvt_pk_bf16_f32 v20, v20, v21
	v_cvt_pk_bf16_f32 v21, v32, v33
	global_store_dwordx4 v[28:29], v[18:21], off offset:256
	v_add_u32_e32 v3, 16, v16
	v_cvt_f32_i32_e32 v3, v3
	ds_read_b128 v[18:21], v13 offset:512
	v_mul_f32_e32 v28, v26, v3
	v_mul_f32_e32 v17, v24, v3
	v_cos_f32_e32 v23, v28
	v_sin_f32_e32 v33, v28
	s_waitcnt lgkmcnt(0)
	v_mov_b32_e32 v28, v19
	v_mov_b32_e32 v29, v20
	v_mov_b32_e32 v19, v21
	v_cos_f32_e32 v22, v17
	v_sin_f32_e32 v32, v17
	v_mul_f32_e32 v17, v27, v3
	v_pk_add_f32 v[18:19], v[28:29], v[18:19]
	v_cos_f32_e32 v34, v17
	v_sin_f32_e32 v36, v17
	v_add_f32_e32 v17, v18, v19
	v_fmamk_f32 v17, v17, 0x37000000, v222
	v_rsq_f32_e32 v17, v17
	v_mul_f32_e32 v3, v25, v3
	v_sin_f32_e32 v37, v3
	v_cos_f32_e32 v35, v3
	v_mul_f32_e32 v18, 0x3d000000, v17
	v_pk_mul_f32 v[20:21], v[10:11], v[18:19] op_sel_hi:[1,0]
	v_pk_mul_f32 v[28:29], v[8:9], v[18:19] op_sel_hi:[1,0]
	v_pk_mul_f32 v[30:31], v[4:5], v[18:19] op_sel_hi:[1,0]
	v_pk_mul_f32 v[18:19], v[6:7], v[18:19] op_sel_hi:[1,0]
	v_pk_mul_f32 v[30:31], v[170:171], v[30:31]
	v_pk_mul_f32 v[18:19], v[172:173], v[18:19]
	v_pk_mul_f32 v[28:29], v[178:179], v[28:29]
	v_pk_mul_f32 v[20:21], v[180:181], v[20:21]
	v_pk_mul_f32 v[38:39], v[32:33], v[30:31]
	v_pk_mul_f32 v[40:41], v[36:37], v[18:19]
	v_pk_fma_f32 v[38:39], v[22:23], v[28:29], v[38:39] neg_lo:[0,0,1] neg_hi:[0,0,1]
	v_pk_fma_f32 v[40:41], v[34:35], v[20:21], v[40:41] neg_lo:[0,0,1] neg_hi:[0,0,1]
	v_pk_mul_f32 v[28:29], v[32:33], v[28:29]
	v_pk_mul_f32 v[20:21], v[36:37], v[20:21]
	s_nop 0
	v_pk_fma_f32 v[42:43], v[34:35], v[18:19], v[20:21]
	v_pk_fma_f32 v[20:21], v[22:23], v[30:31], v[28:29]
	v_cvt_pk_bf16_f32 v18, v38, v39
	v_cvt_pk_bf16_f32 v19, v40, v41
	v_or_b32_e32 v38, 16, v2
	v_cvt_pk_bf16_f32 v20, v20, v21
	v_cvt_pk_bf16_f32 v21, v42, v43
	ds_read_b128 v[28:31], v13 offset:528
	v_ashrrev_i32_e32 v39, 31, v38
	s_waitcnt lgkmcnt(0)
	v_mov_b32_e32 v40, v29
	v_mov_b32_e32 v41, v30
	v_mov_b32_e32 v29, v31
	v_pk_add_f32 v[28:29], v[40:41], v[28:29]
	s_nop 0
	v_add_f32_e32 v3, v28, v29
	v_fmamk_f32 v3, v3, 0x37000000, v222
	v_rsq_f32_e32 v3, v3
	v_lshlrev_b64 v[28:29], s34, v[38:39]
	v_lshl_add_u64 v[28:29], v[28:29], 1, v[14:15]
	global_store_dwordx4 v[28:29], v[18:21], off
	s_nop 1
	v_mul_f32_e32 v18, 0x3d000000, v3
	v_pk_mul_f32 v[20:21], v[10:11], v[18:19] op_sel_hi:[1,0]
	v_pk_mul_f32 v[30:31], v[8:9], v[18:19] op_sel_hi:[1,0]
	v_pk_mul_f32 v[38:39], v[4:5], v[18:19] op_sel_hi:[1,0]
	v_pk_mul_f32 v[18:19], v[6:7], v[18:19] op_sel_hi:[1,0]
	v_pk_mul_f32 v[38:39], v[158:159], v[38:39]
	v_pk_mul_f32 v[18:19], v[160:161], v[18:19]
	v_pk_mul_f32 v[30:31], v[166:167], v[30:31]
	v_pk_mul_f32 v[20:21], v[168:169], v[20:21]
	v_pk_mul_f32 v[40:41], v[32:33], v[38:39]
	v_pk_mul_f32 v[42:43], v[36:37], v[18:19]
	v_pk_fma_f32 v[40:41], v[22:23], v[30:31], v[40:41] neg_lo:[0,0,1] neg_hi:[0,0,1]
	v_pk_fma_f32 v[42:43], v[34:35], v[20:21], v[42:43] neg_lo:[0,0,1] neg_hi:[0,0,1]
	v_pk_mul_f32 v[30:31], v[32:33], v[30:31]
	v_pk_mul_f32 v[20:21], v[36:37], v[20:21]
	s_nop 0
	v_pk_fma_f32 v[44:45], v[34:35], v[18:19], v[20:21]
	v_pk_fma_f32 v[20:21], v[22:23], v[38:39], v[30:31]
	v_cvt_pk_bf16_f32 v18, v40, v41
	v_cvt_pk_bf16_f32 v19, v42, v43
	s_nop 0
	v_cvt_pk_bf16_f32 v20, v20, v21
	v_cvt_pk_bf16_f32 v21, v44, v45
	global_store_dwordx4 v[28:29], v[18:21], off offset:256
	ds_read_b128 v[18:21], v13 offset:4608
	s_waitcnt lgkmcnt(0)
	v_mov_b32_e32 v28, v19
	v_mov_b32_e32 v29, v20
	v_mov_b32_e32 v19, v21
	v_pk_add_f32 v[18:19], v[28:29], v[18:19]
	s_nop 0
	v_add_f32_e32 v3, v18, v19
	v_fmamk_f32 v3, v3, 0x37000000, v222
	v_rsq_f32_e32 v3, v3
	s_nop 0
	v_mul_f32_e32 v18, 0x3d000000, v3
	v_pk_mul_f32 v[20:21], v[10:11], v[18:19] op_sel_hi:[1,0]
	v_pk_mul_f32 v[28:29], v[8:9], v[18:19] op_sel_hi:[1,0]
	v_pk_mul_f32 v[30:31], v[4:5], v[18:19] op_sel_hi:[1,0]
	v_pk_mul_f32 v[18:19], v[6:7], v[18:19] op_sel_hi:[1,0]
	v_pk_mul_f32 v[30:31], v[106:107], v[30:31]
	v_pk_mul_f32 v[18:19], v[108:109], v[18:19]
	v_pk_mul_f32 v[28:29], v[114:115], v[28:29]
	v_pk_mul_f32 v[20:21], v[116:117], v[20:21]
	v_pk_mul_f32 v[38:39], v[32:33], v[30:31]
	v_pk_mul_f32 v[40:41], v[36:37], v[18:19]
	v_pk_fma_f32 v[38:39], v[22:23], v[28:29], v[38:39] neg_lo:[0,0,1] neg_hi:[0,0,1]
	v_pk_fma_f32 v[40:41], v[34:35], v[20:21], v[40:41] neg_lo:[0,0,1] neg_hi:[0,0,1]
	v_pk_mul_f32 v[28:29], v[32:33], v[28:29]
	v_pk_mul_f32 v[20:21], v[36:37], v[20:21]
	s_nop 0
	v_pk_fma_f32 v[42:43], v[34:35], v[18:19], v[20:21]
	v_pk_fma_f32 v[20:21], v[22:23], v[30:31], v[28:29]
	v_cvt_pk_bf16_f32 v18, v38, v39
	v_cvt_pk_bf16_f32 v19, v40, v41
	v_add_u32_e32 v38, 0x90, v2
	v_cvt_pk_bf16_f32 v20, v20, v21
	v_cvt_pk_bf16_f32 v21, v42, v43
	ds_read_b128 v[28:31], v13 offset:4624
	v_ashrrev_i32_e32 v39, 31, v38
	s_waitcnt lgkmcnt(0)
;     DI void operator()(const f32x4 (&acc)[2][2][4][2], const Unit& u, int wr, int wc, int fr, int fq) const {
;     ...
;             for (int m = 0; m < 4; ++m) { const float pos = (float)(16 * m + fro); f32x4 cs, sn;
; #pragma unroll
;                 for (int j = 0; j < 4; ++j) { const float rev = pos * ifr[j]; cs[j] = __builtin_amdgcn_cosf(rev); sn[j] = __builtin_amdgcn_sinf(rev); }
; #pragma unroll
;                 for (int ai = 0; ai < 2; ++ai) QKV_OUT(ai, m, cs, sn); }
	v_mov_b32_e32 v40, v29
	v_mov_b32_e32 v41, v30
	v_mov_b32_e32 v29, v31
	v_pk_add_f32 v[28:29], v[40:41], v[28:29]
	s_nop 0
	v_add_f32_e32 v3, v28, v29
	v_fmamk_f32 v3, v3, 0x37000000, v222
	v_rsq_f32_e32 v3, v3
	v_lshlrev_b64 v[28:29], s34, v[38:39]
	v_lshl_add_u64 v[28:29], v[28:29], 1, v[14:15]
	global_store_dwordx4 v[28:29], v[18:21], off
	s_nop 1
	v_mul_f32_e32 v18, 0x3d000000, v3
	v_pk_mul_f32 v[20:21], v[10:11], v[18:19] op_sel_hi:[1,0]
	v_pk_mul_f32 v[30:31], v[8:9], v[18:19] op_sel_hi:[1,0]
	v_pk_mul_f32 v[38:39], v[4:5], v[18:19] op_sel_hi:[1,0]
	v_pk_mul_f32 v[18:19], v[6:7], v[18:19] op_sel_hi:[1,0]
	v_pk_mul_f32 v[38:39], v[74:75], v[38:39]
	v_pk_mul_f32 v[18:19], v[76:77], v[18:19]
	v_pk_mul_f32 v[30:31], v[86:87], v[30:31]
	v_pk_mul_f32 v[20:21], v[88:89], v[20:21]
	v_pk_mul_f32 v[40:41], v[32:33], v[38:39]
	v_pk_mul_f32 v[42:43], v[36:37], v[18:19]
	v_pk_fma_f32 v[40:41], v[22:23], v[30:31], v[40:41] neg_lo:[0,0,1] neg_hi:[0,0,1]
	v_pk_fma_f32 v[42:43], v[34:35], v[20:21], v[42:43] neg_lo:[0,0,1] neg_hi:[0,0,1]
	v_pk_mul_f32 v[30:31], v[32:33], v[30:31]
	v_pk_mul_f32 v[20:21], v[36:37], v[20:21]
	s_nop 0
	v_pk_fma_f32 v[32:33], v[34:35], v[18:19], v[20:21]
	v_pk_fma_f32 v[20:21], v[22:23], v[38:39], v[30:31]
	v_cvt_pk_bf16_f32 v18, v40, v41
	v_cvt_pk_bf16_f32 v19, v42, v43
	s_nop 0
	v_cvt_pk_bf16_f32 v20, v20, v21
	v_cvt_pk_bf16_f32 v21, v32, v33
	global_store_dwordx4 v[28:29], v[18:21], off offset:256
	v_add_u32_e32 v3, 32, v16
	v_cvt_f32_i32_e32 v3, v3
	ds_read_b128 v[18:21], v13 offset:1024
	v_mul_f32_e32 v28, v26, v3
	v_mul_f32_e32 v17, v24, v3
	v_cos_f32_e32 v23, v28
	v_sin_f32_e32 v33, v28
	s_waitcnt lgkmcnt(0)
	v_mov_b32_e32 v28, v19
	v_mov_b32_e32 v29, v20
	v_mov_b32_e32 v19, v21
	v_cos_f32_e32 v22, v17
	v_sin_f32_e32 v32, v17
	v_mul_f32_e32 v17, v27, v3
	v_pk_add_f32 v[18:19], v[28:29], v[18:19]
	v_cos_f32_e32 v34, v17
	v_sin_f32_e32 v36, v17
	v_add_f32_e32 v17, v18, v19
	v_fmamk_f32 v17, v17, 0x37000000, v222
	v_rsq_f32_e32 v17, v17
	v_mul_f32_e32 v3, v25, v3
	v_sin_f32_e32 v37, v3
	v_cos_f32_e32 v35, v3
	v_mul_f32_e32 v18, 0x3d000000, v17
	v_pk_mul_f32 v[20:21], v[10:11], v[18:19] op_sel_hi:[1,0]
	v_pk_mul_f32 v[28:29], v[8:9], v[18:19] op_sel_hi:[1,0]
	v_pk_mul_f32 v[30:31], v[4:5], v[18:19] op_sel_hi:[1,0]
	v_pk_mul_f32 v[18:19], v[6:7], v[18:19] op_sel_hi:[1,0]
	v_pk_mul_f32 v[30:31], v[154:155], v[30:31]
	v_pk_mul_f32 v[18:19], v[156:157], v[18:19]
	v_pk_mul_f32 v[28:29], v[162:163], v[28:29]
	v_pk_mul_f32 v[20:21], v[164:165], v[20:21]
	v_pk_mul_f32 v[38:39], v[32:33], v[30:31]
	v_pk_mul_f32 v[40:41], v[36:37], v[18:19]
	v_pk_fma_f32 v[38:39], v[22:23], v[28:29], v[38:39] neg_lo:[0,0,1] neg_hi:[0,0,1]
	v_pk_fma_f32 v[40:41], v[34:35], v[20:21], v[40:41] neg_lo:[0,0,1] neg_hi:[0,0,1]
	v_pk_mul_f32 v[28:29], v[32:33], v[28:29]
	v_pk_mul_f32 v[20:21], v[36:37], v[20:21]
	s_nop 0
	v_pk_fma_f32 v[42:43], v[34:35], v[18:19], v[20:21]
	v_pk_fma_f32 v[20:21], v[22:23], v[30:31], v[28:29]
	v_cvt_pk_bf16_f32 v18, v38, v39
	v_cvt_pk_bf16_f32 v19, v40, v41
	v_or_b32_e32 v38, 32, v2
	v_cvt_pk_bf16_f32 v20, v20, v21
	v_cvt_pk_bf16_f32 v21, v42, v43
	ds_read_b128 v[28:31], v13 offset:1040
	v_ashrrev_i32_e32 v39, 31, v38
	s_waitcnt lgkmcnt(0)
	v_mov_b32_e32 v40, v29
	v_mov_b32_e32 v41, v30
	v_mov_b32_e32 v29, v31
	v_pk_add_f32 v[28:29], v[40:41], v[28:29]
	s_nop 0
	v_add_f32_e32 v3, v28, v29
	v_fmamk_f32 v3, v3, 0x37000000, v222
	v_rsq_f32_e32 v3, v3
	v_lshlrev_b64 v[28:29], s34, v[38:39]
	v_lshl_add_u64 v[28:29], v[28:29], 1, v[14:15]
	global_store_dwordx4 v[28:29], v[18:21], off
	s_nop 1
	v_mul_f32_e32 v18, 0x3d000000, v3
	v_pk_mul_f32 v[20:21], v[10:11], v[18:19] op_sel_hi:[1,0]
	v_pk_mul_f32 v[30:31], v[8:9], v[18:19] op_sel_hi:[1,0]
	v_pk_mul_f32 v[38:39], v[4:5], v[18:19] op_sel_hi:[1,0]
	v_pk_mul_f32 v[18:19], v[6:7], v[18:19] op_sel_hi:[1,0]
	v_pk_mul_f32 v[38:39], v[142:143], v[38:39]
	v_pk_mul_f32 v[18:19], v[144:145], v[18:19]
	v_pk_mul_f32 v[30:31], v[150:151], v[30:31]
	v_pk_mul_f32 v[20:21], v[152:153], v[20:21]
	v_pk_mul_f32 v[40:41], v[32:33], v[38:39]
	v_pk_mul_f32 v[42:43], v[36:37], v[18:19]
	v_pk_fma_f32 v[40:41], v[22:23], v[30:31], v[40:41] neg_lo:[0,0,1] neg_hi:[0,0,1]
	v_pk_fma_f32 v[42:43], v[34:35], v[20:21], v[42:43] neg_lo:[0,0,1] neg_hi:[0,0,1]
	v_pk_mul_f32 v[30:31], v[32:33], v[30:31]
	v_pk_mul_f32 v[20:21], v[36:37], v[20:21]
	s_nop 0
	v_pk_fma_f32 v[44:45], v[34:35], v[18:19], v[20:21]
	v_pk_fma_f32 v[20:21], v[22:23], v[38:39], v[30:31]
	v_cvt_pk_bf16_f32 v18, v40, v41
	v_cvt_pk_bf16_f32 v19, v42, v43
	s_nop 0
	v_cvt_pk_bf16_f32 v20, v20, v21
	v_cvt_pk_bf16_f32 v21, v44, v45
	global_store_dwordx4 v[28:29], v[18:21], off offset:256
	ds_read_b128 v[18:21], v13 offset:5120
	s_waitcnt lgkmcnt(0)
	v_mov_b32_e32 v28, v19
	v_mov_b32_e32 v29, v20
	v_mov_b32_e32 v19, v21
	v_pk_add_f32 v[18:19], v[28:29], v[18:19]
	s_nop 0
	v_add_f32_e32 v3, v18, v19
	v_fmamk_f32 v3, v3, 0x37000000, v222
	v_rsq_f32_e32 v3, v3
	s_nop 0
	v_mul_f32_e32 v18, 0x3d000000, v3
	v_pk_mul_f32 v[20:21], v[10:11], v[18:19] op_sel_hi:[1,0]
	v_pk_mul_f32 v[28:29], v[8:9], v[18:19] op_sel_hi:[1,0]
	v_pk_mul_f32 v[30:31], v[4:5], v[18:19] op_sel_hi:[1,0]
	v_pk_mul_f32 v[18:19], v[6:7], v[18:19] op_sel_hi:[1,0]
	v_pk_mul_f32 v[30:31], v[78:79], v[30:31]
	v_pk_mul_f32 v[18:19], v[80:81], v[18:19]
	v_pk_mul_f32 v[28:29], v[82:83], v[28:29]
	v_pk_mul_f32 v[20:21], v[84:85], v[20:21]
	v_pk_mul_f32 v[38:39], v[32:33], v[30:31]
	v_pk_mul_f32 v[40:41], v[36:37], v[18:19]
	v_pk_fma_f32 v[38:39], v[22:23], v[28:29], v[38:39] neg_lo:[0,0,1] neg_hi:[0,0,1]
	v_pk_fma_f32 v[40:41], v[34:35], v[20:21], v[40:41] neg_lo:[0,0,1] neg_hi:[0,0,1]
	v_pk_mul_f32 v[28:29], v[32:33], v[28:29]
	v_pk_mul_f32 v[20:21], v[36:37], v[20:21]
	s_nop 0
	v_pk_fma_f32 v[42:43], v[34:35], v[18:19], v[20:21]
	v_pk_fma_f32 v[20:21], v[22:23], v[30:31], v[28:29]
	v_cvt_pk_bf16_f32 v18, v38, v39
	v_cvt_pk_bf16_f32 v19, v40, v41
	v_add_u32_e32 v38, 0xa0, v2
	v_cvt_pk_bf16_f32 v20, v20, v21
	v_cvt_pk_bf16_f32 v21, v42, v43
	ds_read_b128 v[28:31], v13 offset:5136
	v_ashrrev_i32_e32 v39, 31, v38
	s_waitcnt lgkmcnt(0)
;     DI void operator()(const f32x4 (&acc)[2][2][4][2], const Unit& u, int wr, int wc, int fr, int fq) const {
;     ...
;             for (int m = 0; m < 4; ++m) { const float pos = (float)(16 * m + fro); f32x4 cs, sn;
; #pragma unroll
;                 for (int j = 0; j < 4; ++j) { const float rev = pos * ifr[j]; cs[j] = __builtin_amdgcn_cosf(rev); sn[j] = __builtin_amdgcn_sinf(rev); }
; #pragma unroll
;                 for (int ai = 0; ai < 2; ++ai) QKV_OUT(ai, m, cs, sn); }
	v_mov_b32_e32 v40, v29
	v_mov_b32_e32 v41, v30
	v_mov_b32_e32 v29, v31
	v_pk_add_f32 v[28:29], v[40:41], v[28:29]
	s_nop 0
	v_add_f32_e32 v3, v28, v29
	v_fmamk_f32 v3, v3, 0x37000000, v222
	v_rsq_f32_e32 v3, v3
	v_lshlrev_b64 v[28:29], s34, v[38:39]
	v_lshl_add_u64 v[28:29], v[28:29], 1, v[14:15]
	global_store_dwordx4 v[28:29], v[18:21], off
	s_nop 1
	v_mul_f32_e32 v18, 0x3d000000, v3
	v_pk_mul_f32 v[20:21], v[10:11], v[18:19] op_sel_hi:[1,0]
	v_pk_mul_f32 v[30:31], v[8:9], v[18:19] op_sel_hi:[1,0]
	v_pk_mul_f32 v[38:39], v[4:5], v[18:19] op_sel_hi:[1,0]
	v_pk_mul_f32 v[18:19], v[6:7], v[18:19] op_sel_hi:[1,0]
	v_pk_mul_f32 v[38:39], v[102:103], v[38:39]
	v_pk_mul_f32 v[18:19], v[104:105], v[18:19]
	v_pk_mul_f32 v[30:31], v[98:99], v[30:31]
	v_pk_mul_f32 v[20:21], v[100:101], v[20:21]
	v_pk_mul_f32 v[40:41], v[32:33], v[38:39]
	v_pk_mul_f32 v[42:43], v[36:37], v[18:19]
	v_pk_fma_f32 v[40:41], v[22:23], v[30:31], v[40:41] neg_lo:[0,0,1] neg_hi:[0,0,1]
	v_pk_fma_f32 v[42:43], v[34:35], v[20:21], v[42:43] neg_lo:[0,0,1] neg_hi:[0,0,1]
	v_pk_mul_f32 v[30:31], v[32:33], v[30:31]
	v_pk_mul_f32 v[20:21], v[36:37], v[20:21]
	s_nop 0
	v_pk_fma_f32 v[32:33], v[34:35], v[18:19], v[20:21]
	v_pk_fma_f32 v[20:21], v[22:23], v[38:39], v[30:31]
	v_cvt_pk_bf16_f32 v18, v40, v41
	v_cvt_pk_bf16_f32 v19, v42, v43
	s_nop 0
	v_cvt_pk_bf16_f32 v20, v20, v21
	v_cvt_pk_bf16_f32 v21, v32, v33
	global_store_dwordx4 v[28:29], v[18:21], off offset:256
	v_add_u32_e32 v3, 48, v16
	v_cvt_f32_i32_e32 v3, v3
	v_mul_f32_e32 v16, v24, v3
	v_cos_f32_e32 v28, v16
	v_sin_f32_e32 v30, v16
	ds_read_b128 v[16:19], v13 offset:1536
	v_mul_f32_e32 v20, v26, v3
	v_cos_f32_e32 v29, v20
	v_sin_f32_e32 v31, v20
	v_mul_f32_e32 v20, v27, v3
	v_cos_f32_e32 v32, v20
	v_sin_f32_e32 v34, v20
	s_waitcnt lgkmcnt(0)
	v_mov_b32_e32 v20, v17
	v_mov_b32_e32 v21, v18
	v_mov_b32_e32 v17, v19
	v_pk_add_f32 v[16:17], v[20:21], v[16:17]
	v_mul_f32_e32 v3, v25, v3
	v_add_f32_e32 v16, v16, v17
	v_fmamk_f32 v16, v16, 0x37000000, v222
	v_rsq_f32_e32 v16, v16
	v_sin_f32_e32 v35, v3
	v_cos_f32_e32 v33, v3
	v_mul_f32_e32 v16, 0x3d000000, v16
	v_pk_mul_f32 v[18:19], v[10:11], v[16:17] op_sel_hi:[1,0]
	v_pk_mul_f32 v[20:21], v[8:9], v[16:17] op_sel_hi:[1,0]
	v_pk_mul_f32 v[22:23], v[4:5], v[16:17] op_sel_hi:[1,0]
	v_pk_mul_f32 v[16:17], v[6:7], v[16:17] op_sel_hi:[1,0]
	v_pk_mul_f32 v[22:23], v[138:139], v[22:23]
	v_pk_mul_f32 v[16:17], v[140:141], v[16:17]
	v_pk_mul_f32 v[20:21], v[146:147], v[20:21]
	v_pk_mul_f32 v[18:19], v[148:149], v[18:19]
	v_pk_mul_f32 v[36:37], v[30:31], v[22:23]
	v_pk_mul_f32 v[38:39], v[34:35], v[16:17]
	v_pk_fma_f32 v[36:37], v[28:29], v[20:21], v[36:37] neg_lo:[0,0,1] neg_hi:[0,0,1]
	v_pk_fma_f32 v[38:39], v[32:33], v[18:19], v[38:39] neg_lo:[0,0,1] neg_hi:[0,0,1]
	v_pk_mul_f32 v[20:21], v[30:31], v[20:21]
	v_pk_mul_f32 v[18:19], v[34:35], v[18:19]
	s_nop 0
	v_pk_fma_f32 v[40:41], v[32:33], v[16:17], v[18:19]
	v_pk_fma_f32 v[18:19], v[28:29], v[22:23], v[20:21]
	v_cvt_pk_bf16_f32 v16, v36, v37
	v_cvt_pk_bf16_f32 v17, v38, v39
	v_or_b32_e32 v36, 48, v2
	v_cvt_pk_bf16_f32 v18, v18, v19
	v_cvt_pk_bf16_f32 v19, v40, v41
	ds_read_b128 v[20:23], v13 offset:1552
	v_ashrrev_i32_e32 v37, 31, v36
	s_waitcnt lgkmcnt(0)
;     DI void operator()(const f32x4 (&acc)[2][2][4][2], const Unit& u, int wr, int wc, int fr, int fq) const {
;     ...
;             for (int m = 0; m < 4; ++m) { const float pos = (float)(16 * m + fro); f32x4 cs, sn;
; #pragma unroll
;                 for (int j = 0; j < 4; ++j) { const float rev = pos * ifr[j]; cs[j] = __builtin_amdgcn_cosf(rev); sn[j] = __builtin_amdgcn_sinf(rev); }
; #pragma unroll
;                 for (int ai = 0; ai < 2; ++ai) QKV_OUT(ai, m, cs, sn); }
	v_mov_b32_e32 v38, v21
	v_mov_b32_e32 v39, v22
	v_mov_b32_e32 v21, v23
	v_pk_add_f32 v[20:21], v[38:39], v[20:21]
	s_nop 0
	v_add_f32_e32 v3, v20, v21
	v_fmamk_f32 v3, v3, 0x37000000, v222
	v_rsq_f32_e32 v3, v3
	v_lshlrev_b64 v[20:21], s34, v[36:37]
	v_lshl_add_u64 v[20:21], v[20:21], 1, v[14:15]
	global_store_dwordx4 v[20:21], v[16:19], off
	s_nop 1
	v_mul_f32_e32 v16, 0x3d000000, v3
	v_pk_mul_f32 v[18:19], v[10:11], v[16:17] op_sel_hi:[1,0]
	v_pk_mul_f32 v[22:23], v[8:9], v[16:17] op_sel_hi:[1,0]
	v_pk_mul_f32 v[36:37], v[4:5], v[16:17] op_sel_hi:[1,0]
	v_pk_mul_f32 v[16:17], v[6:7], v[16:17] op_sel_hi:[1,0]
	v_pk_mul_f32 v[36:37], v[130:131], v[36:37]
	v_pk_mul_f32 v[16:17], v[132:133], v[16:17]
	v_pk_mul_f32 v[22:23], v[134:135], v[22:23]
	v_pk_mul_f32 v[18:19], v[136:137], v[18:19]
	v_pk_mul_f32 v[38:39], v[30:31], v[36:37]
	v_pk_mul_f32 v[40:41], v[34:35], v[16:17]
	v_pk_fma_f32 v[38:39], v[28:29], v[22:23], v[38:39] neg_lo:[0,0,1] neg_hi:[0,0,1]
	v_pk_fma_f32 v[40:41], v[32:33], v[18:19], v[40:41] neg_lo:[0,0,1] neg_hi:[0,0,1]
	v_pk_mul_f32 v[22:23], v[30:31], v[22:23]
	v_pk_mul_f32 v[18:19], v[34:35], v[18:19]
	s_nop 0
	v_pk_fma_f32 v[42:43], v[32:33], v[16:17], v[18:19]
	v_pk_fma_f32 v[18:19], v[28:29], v[36:37], v[22:23]
	v_cvt_pk_bf16_f32 v16, v38, v39
	v_cvt_pk_bf16_f32 v17, v40, v41
	s_nop 0
	v_cvt_pk_bf16_f32 v18, v18, v19
	v_cvt_pk_bf16_f32 v19, v42, v43
	global_store_dwordx4 v[20:21], v[16:19], off offset:256
	ds_read_b128 v[16:19], v13 offset:5632
	s_waitcnt lgkmcnt(0)
	v_mov_b32_e32 v20, v17
	v_mov_b32_e32 v21, v18
	v_mov_b32_e32 v17, v19
	v_pk_add_f32 v[16:17], v[20:21], v[16:17]
	s_nop 0
	v_add_f32_e32 v3, v16, v17
	v_fmamk_f32 v3, v3, 0x37000000, v222
	v_rsq_f32_e32 v3, v3
	s_nop 0
	v_mul_f32_e32 v16, 0x3d000000, v3
	v_pk_mul_f32 v[18:19], v[10:11], v[16:17] op_sel_hi:[1,0]
	v_pk_mul_f32 v[20:21], v[8:9], v[16:17] op_sel_hi:[1,0]
	v_pk_mul_f32 v[22:23], v[4:5], v[16:17] op_sel_hi:[1,0]
	v_pk_mul_f32 v[16:17], v[6:7], v[16:17] op_sel_hi:[1,0]
	v_pk_mul_f32 v[22:23], v[66:67], v[22:23]
	v_pk_mul_f32 v[16:17], v[68:69], v[16:17]
	v_pk_mul_f32 v[20:21], v[70:71], v[20:21]
	v_pk_mul_f32 v[18:19], v[72:73], v[18:19]
	v_pk_mul_f32 v[36:37], v[30:31], v[22:23]
	v_pk_mul_f32 v[38:39], v[34:35], v[16:17]
	v_pk_fma_f32 v[36:37], v[28:29], v[20:21], v[36:37] neg_lo:[0,0,1] neg_hi:[0,0,1]
	v_pk_fma_f32 v[38:39], v[32:33], v[18:19], v[38:39] neg_lo:[0,0,1] neg_hi:[0,0,1]
	v_pk_mul_f32 v[20:21], v[30:31], v[20:21]
	v_pk_mul_f32 v[18:19], v[34:35], v[18:19]
	s_nop 0
	v_pk_fma_f32 v[40:41], v[32:33], v[16:17], v[18:19]
	v_pk_fma_f32 v[18:19], v[28:29], v[22:23], v[20:21]
	v_cvt_pk_bf16_f32 v16, v36, v37
	v_cvt_pk_bf16_f32 v17, v38, v39
	v_add_u32_e32 v36, 0xb0, v2
	v_cvt_pk_bf16_f32 v18, v18, v19
	v_cvt_pk_bf16_f32 v19, v40, v41
	ds_read_b128 v[20:23], v13 offset:5648
	v_ashrrev_i32_e32 v37, 31, v36
	s_waitcnt lgkmcnt(0)
	v_mov_b32_e32 v38, v21
	v_mov_b32_e32 v39, v22
	v_mov_b32_e32 v21, v23
	v_pk_add_f32 v[20:21], v[38:39], v[20:21]
	s_nop 0
	v_add_f32_e32 v3, v20, v21
	v_fmamk_f32 v3, v3, 0x37000000, v222
	v_rsq_f32_e32 v3, v3
	v_lshlrev_b64 v[20:21], s34, v[36:37]
	v_lshl_add_u64 v[20:21], v[20:21], 1, v[14:15]
	global_store_dwordx4 v[20:21], v[16:19], off
	s_nop 1
	v_mul_f32_e32 v16, 0x3d000000, v3
	v_pk_mul_f32 v[18:19], v[10:11], v[16:17] op_sel_hi:[1,0]
	v_pk_mul_f32 v[22:23], v[8:9], v[16:17] op_sel_hi:[1,0]
	v_pk_mul_f32 v[36:37], v[4:5], v[16:17] op_sel_hi:[1,0]
	v_pk_mul_f32 v[16:17], v[6:7], v[16:17] op_sel_hi:[1,0]
	v_pk_mul_f32 v[36:37], v[94:95], v[36:37]
	v_pk_mul_f32 v[16:17], v[96:97], v[16:17]
	v_pk_mul_f32 v[22:23], v[90:91], v[22:23]
	v_pk_mul_f32 v[18:19], v[92:93], v[18:19]
	v_pk_mul_f32 v[38:39], v[30:31], v[36:37]
	v_pk_mul_f32 v[40:41], v[34:35], v[16:17]
	v_pk_fma_f32 v[38:39], v[28:29], v[22:23], v[38:39] neg_lo:[0,0,1] neg_hi:[0,0,1]
	v_pk_fma_f32 v[40:41], v[32:33], v[18:19], v[40:41] neg_lo:[0,0,1] neg_hi:[0,0,1]
	v_pk_mul_f32 v[22:23], v[30:31], v[22:23]
	v_pk_mul_f32 v[18:19], v[34:35], v[18:19]
	s_nop 0
	v_pk_fma_f32 v[30:31], v[32:33], v[16:17], v[18:19]
	v_pk_fma_f32 v[18:19], v[28:29], v[36:37], v[22:23]
	v_cvt_pk_bf16_f32 v16, v38, v39
	v_cvt_pk_bf16_f32 v17, v40, v41
	s_nop 0
	v_cvt_pk_bf16_f32 v18, v18, v19
	v_cvt_pk_bf16_f32 v19, v30, v31
	global_store_dwordx4 v[20:21], v[16:19], off offset:256
	s_mov_b64 s[28:29], 0
